# baseline (speedup 1.0000x reference)
_Z11prep_kernelPKfS0_S0_S0_S0_S0_S0_S0_S0_PKiPDv8_DF16bS4_PfS5_S5_PiPt:
	s_load_dwordx4 s[16:19], s[0:1], 0x0
	s_load_dwordx4 s[20:23], s[0:1], 0x10
	s_load_dwordx4 s[24:27], s[0:1], 0x20
	s_load_dwordx4 s[28:31], s[0:1], 0x30
	s_load_dwordx4 s[32:35], s[0:1], 0x40
	s_load_dwordx2 s[36:37], s[0:1], 0x80
	v_and_b32_e32 v126, 63, v0
	v_lshrrev_b32_e32 v128, 6, v0
	v_and_b32_e32 v1, 15, v0
	v_bfe_u32 v24, v0, 4, 2
	v_lshl_or_b32 v107, v128, 4, v1
	v_lshlrev_b32_e32 v106, 2, v107
	v_lshlrev_b32_e32 v127, 2, v0
	v_lshlrev_b32_e32 v25, 1, v107
	v_and_b32_e32 v26, 48, v0
	v_mul_u32_u24_e32 v27, 0x440, v24
	v_lshlrev_b32_e32 v120, 4, v0
	v_lshrrev_b32_e32 v58, 5, v0
	v_mul_u32_u24_e32 v58, 0x110, v58
	v_and_b32_e32 v125, 31, v0
	v_lshl_add_u32 v58, v125, 3, v58
	v_add_u32_e32 v124, 0x1b400, v58
	v_mul_u32_u24_e32 v52, 0x110, v1
	v_add_u32_e32 v52, v52, v26
	v_add_u32_e32 v53, 0x1b400, v52
	v_add_u32_e32 v54, 0x1c500, v52
	v_add_u32_e32 v55, v27, v25
	v_add_u32_e32 v55, 0x1c500, v55
	v_mul_u32_u24_e32 v56, 0x110, v107
	v_add_u32_e32 v56, v56, v26
	v_add_u32_e32 v57, 0x8800, v56
	s_lshl_b32 s12, s2, 4
	s_add_i32 s3, s12, 0xfffff800
	s_cmpk_gt_i32 s2, 0x7f
	s_cselect_b64 s[6:7], -1, 0
	s_mov_b32 s48, 0
	s_mov_b32 s49, -1
	v_lshl_or_b32 v123, s2, 3, v128
	v_lshlrev_b32_e32 v123, 12, v123
	v_lshl_add_u32 v123, v126, 4, v123
	s_waitcnt lgkmcnt(0)
	s_cmpk_lt_i32 s2, 0x80
	s_cselect_b32 s38, s16, s18
	s_cselect_b32 s39, s17, s19
	s_cselect_b32 s40, s20, s24
	s_cselect_b32 s41, s21, s25
	s_cselect_b32 s13, s12, s3
	s_cselect_b32 s44, 0x3db504f3, 1.0
	s_lshl_b32 s13, s13, 9
	s_add_u32 s38, s38, s13
	s_addc_u32 s39, s39, 0
	global_load_dwordx4 v[2:5], v120, s[38:39] nt
	s_and_b32 s13, s2, 7
	s_lshl_b32 s14, s13, 13
	v_add_u32_e32 v125, s14, v120
	global_load_dwordx4 v[80:83], v125, s[40:41]
	s_add_i32 s13, s2, 1
	s_and_b32 s13, s13, 7
	s_lshl_b32 s14, s13, 13
	v_add_u32_e32 v125, s14, v120
	global_load_dwordx4 v[84:87], v125, s[40:41]
	s_add_i32 s13, s2, 2
	s_and_b32 s13, s13, 7
	s_lshl_b32 s14, s13, 13
	v_add_u32_e32 v125, s14, v120
	global_load_dwordx4 v[88:91], v125, s[40:41]
	s_add_i32 s13, s2, 3
	s_and_b32 s13, s13, 7
	s_lshl_b32 s14, s13, 13
	v_add_u32_e32 v125, s14, v120
	global_load_dwordx4 v[92:95], v125, s[40:41]
	s_add_i32 s13, s2, 4
	s_and_b32 s13, s13, 7
	s_lshl_b32 s14, s13, 13
	v_add_u32_e32 v125, s14, v120
	global_load_dwordx4 v[96:99], v125, s[40:41]
	s_add_i32 s13, s2, 5
	s_and_b32 s13, s13, 7
	s_lshl_b32 s14, s13, 13
	v_add_u32_e32 v125, s14, v120
	global_load_dwordx4 v[100:103], v125, s[40:41]
	s_add_i32 s13, s2, 6
	s_and_b32 s13, s13, 7
	s_lshl_b32 s14, s13, 13
	v_add_u32_e32 v125, s14, v120
	global_load_dwordx4 v[108:111], v125, s[40:41]
	s_add_i32 s13, s2, 7
	s_and_b32 s13, s13, 7
	s_lshl_b32 s14, s13, 13
	v_add_u32_e32 v125, s14, v120
	global_load_dwordx4 v[112:115], v125, s[40:41]
	global_load_dword v129, v106, s[32:33]
	global_load_dword v130, v106, s[30:31]
	s_and_b64 vcc, exec, s[6:7]
	s_cbranch_vccz .Lp_q
	v_cmp_gt_u32_e32 vcc, 32, v126
	v_mov_b32_e32 v198, 0x3db504f3
	v_mov_b32_e32 v125, s22
	v_mov_b32_e32 v104, s26
	v_cndmask_b32_e32 v198, 1.0, v198, vcc
	v_cndmask_b32_e32 v104, v104, v125, vcc
	v_mov_b32_e32 v125, s23
	v_mov_b32_e32 v105, s27
	v_cndmask_b32_e32 v105, v105, v125, vcc
	v_and_b32_e32 v196, 31, v126
	v_lshlrev_b32_e32 v196, 4, v196
	v_mov_b32_e32 v197, 0
	v_lshl_add_u64 v[104:105], v[104:105], 0, v[196:197]
	global_load_dwordx4 v[116:119], v[104:105], off
	v_lshlrev_b32_e32 v121, 14, v128
	v_lshl_add_u32 v121, v126, 4, v121
	s_and_b32 s13, s2, 15
	s_lshl_b32 s14, s13, 10
	s_add_u32 s46, s28, s14
	s_addc_u32 s47, s29, 0
	global_load_dwordx4 v[132:135], v121, s[46:47]
	s_add_i32 s13, s2, 1
	s_and_b32 s13, s13, 15
	s_lshl_b32 s14, s13, 10
	s_add_u32 s46, s28, s14
	s_addc_u32 s47, s29, 0
	global_load_dwordx4 v[136:139], v121, s[46:47]
	s_add_i32 s13, s2, 2
	s_and_b32 s13, s13, 15
	s_lshl_b32 s14, s13, 10
	s_add_u32 s46, s28, s14
	s_addc_u32 s47, s29, 0
	global_load_dwordx4 v[140:143], v121, s[46:47]
	s_add_i32 s13, s2, 3
	s_and_b32 s13, s13, 15
	s_lshl_b32 s14, s13, 10
	s_add_u32 s46, s28, s14
	s_addc_u32 s47, s29, 0
	global_load_dwordx4 v[144:147], v121, s[46:47]
	s_add_i32 s13, s2, 4
	s_and_b32 s13, s13, 15
	s_lshl_b32 s14, s13, 10
	s_add_u32 s46, s28, s14
	s_addc_u32 s47, s29, 0
	global_load_dwordx4 v[148:151], v121, s[46:47]
	s_add_i32 s13, s2, 5
	s_and_b32 s13, s13, 15
	s_lshl_b32 s14, s13, 10
	s_add_u32 s46, s28, s14
	s_addc_u32 s47, s29, 0
	global_load_dwordx4 v[152:155], v121, s[46:47]
	s_add_i32 s13, s2, 6
	s_and_b32 s13, s13, 15
	s_lshl_b32 s14, s13, 10
	s_add_u32 s46, s28, s14
	s_addc_u32 s47, s29, 0
	global_load_dwordx4 v[156:159], v121, s[46:47]
	s_add_i32 s13, s2, 7
	s_and_b32 s13, s13, 15
	s_lshl_b32 s14, s13, 10
	s_add_u32 s46, s28, s14
	s_addc_u32 s47, s29, 0
	global_load_dwordx4 v[160:163], v121, s[46:47]
	s_add_i32 s13, s2, 8
	s_and_b32 s13, s13, 15
	s_lshl_b32 s14, s13, 10
	s_add_u32 s46, s28, s14
	s_addc_u32 s47, s29, 0
	global_load_dwordx4 v[164:167], v121, s[46:47]
	s_add_i32 s13, s2, 9
	s_and_b32 s13, s13, 15
	s_lshl_b32 s14, s13, 10
	s_add_u32 s46, s28, s14
	s_addc_u32 s47, s29, 0
	global_load_dwordx4 v[168:171], v121, s[46:47]
	s_add_i32 s13, s2, 10
	s_and_b32 s13, s13, 15
	s_lshl_b32 s14, s13, 10
	s_add_u32 s46, s28, s14
	s_addc_u32 s47, s29, 0
	global_load_dwordx4 v[172:175], v121, s[46:47]
	s_add_i32 s13, s2, 11
	s_and_b32 s13, s13, 15
	s_lshl_b32 s14, s13, 10
	s_add_u32 s46, s28, s14
	s_addc_u32 s47, s29, 0
	global_load_dwordx4 v[176:179], v121, s[46:47]
	s_add_i32 s13, s2, 12
	s_and_b32 s13, s13, 15
	s_lshl_b32 s14, s13, 10
	s_add_u32 s46, s28, s14
	s_addc_u32 s47, s29, 0
	global_load_dwordx4 v[180:183], v121, s[46:47]
	s_add_i32 s13, s2, 13
	s_and_b32 s13, s13, 15
	s_lshl_b32 s14, s13, 10
	s_add_u32 s46, s28, s14
	s_addc_u32 s47, s29, 0
	global_load_dwordx4 v[184:187], v121, s[46:47]
	s_add_i32 s13, s2, 14
	s_and_b32 s13, s13, 15
	s_lshl_b32 s14, s13, 10
	s_add_u32 s46, s28, s14
	s_addc_u32 s47, s29, 0
	global_load_dwordx4 v[188:191], v121, s[46:47]
	s_add_i32 s13, s2, 15
	s_and_b32 s13, s13, 15
	s_lshl_b32 s14, s13, 10
	s_add_u32 s46, s28, s14
	s_addc_u32 s47, s29, 0
	global_load_dwordx4 v[192:195], v121, s[46:47]
	v_mul_u32_u24_e32 v59, 0x1040, v128
	v_lshl_add_u32 v59, v126, 2, v59
	v_add_u32_e32 v59, 0x11000, v59
	v_mul_u32_u24_e32 v76, 0x1100, v128
	v_lshl_add_u32 v76, v126, 3, v76
	v_add_u32_e32 v76, 0x8700, v76
	v_lshrrev_b32_e32 v77, 2, v126
	v_mul_u32_u24_e32 v77, 0x104, v77
	v_mul_u32_u24_e32 v125, 0x1040, v128
	v_add_u32_e32 v77, v77, v125
	v_and_b32_e32 v125, 3, v126
	v_lshl_add_u32 v77, v125, 6, v77
	v_add_u32_e32 v77, 0x11000, v77
	s_waitcnt vmcnt(27)
	v_cvt_pk_bf16_f32 v12, v2, v3
	v_cvt_pk_bf16_f32 v13, v4, v5
	ds_write_b64 v124, v[12:13]
	s_waitcnt vmcnt(26)
	v_cvt_pk_bf16_f32 v6, v80, v81
	v_cvt_pk_bf16_f32 v7, v82, v83
	s_and_b32 s13, s2, 7
	s_mul_i32 s14, s13, 0x1100
	v_add_u32_e32 v125, s14, v58
	ds_write_b64 v125, v[6:7]
	s_waitcnt vmcnt(25)
	v_cvt_pk_bf16_f32 v8, v84, v85
	v_cvt_pk_bf16_f32 v9, v86, v87
	s_add_i32 s13, s2, 1
	s_and_b32 s13, s13, 7
	s_mul_i32 s14, s13, 0x1100
	v_add_u32_e32 v10, s14, v58
	ds_write_b64 v10, v[8:9]
	s_waitcnt vmcnt(24)
	v_cvt_pk_bf16_f32 v6, v88, v89
	v_cvt_pk_bf16_f32 v7, v90, v91
	s_add_i32 s13, s2, 2
	s_and_b32 s13, s13, 7
	s_mul_i32 s14, s13, 0x1100
	v_add_u32_e32 v125, s14, v58
	ds_write_b64 v125, v[6:7]
	s_waitcnt vmcnt(23)
	v_cvt_pk_bf16_f32 v8, v92, v93
	v_cvt_pk_bf16_f32 v9, v94, v95
	s_add_i32 s13, s2, 3
	s_and_b32 s13, s13, 7
	s_mul_i32 s14, s13, 0x1100
	v_add_u32_e32 v10, s14, v58
	ds_write_b64 v10, v[8:9]
	s_waitcnt vmcnt(22)
	v_cvt_pk_bf16_f32 v6, v96, v97
	v_cvt_pk_bf16_f32 v7, v98, v99
	s_add_i32 s13, s2, 4
	s_and_b32 s13, s13, 7
	s_mul_i32 s14, s13, 0x1100
	v_add_u32_e32 v125, s14, v58
	ds_write_b64 v125, v[6:7]
	s_waitcnt vmcnt(21)
	v_cvt_pk_bf16_f32 v8, v100, v101
	v_cvt_pk_bf16_f32 v9, v102, v103
	s_add_i32 s13, s2, 5
	s_and_b32 s13, s13, 7
	s_mul_i32 s14, s13, 0x1100
	v_add_u32_e32 v10, s14, v58
	ds_write_b64 v10, v[8:9]
	s_waitcnt vmcnt(20)
	v_cvt_pk_bf16_f32 v6, v108, v109
	v_cvt_pk_bf16_f32 v7, v110, v111
	s_add_i32 s13, s2, 6
	s_and_b32 s13, s13, 7
	s_mul_i32 s14, s13, 0x1100
	v_add_u32_e32 v125, s14, v58
	ds_write_b64 v125, v[6:7]
	s_waitcnt vmcnt(19)
	v_cvt_pk_bf16_f32 v8, v112, v113
	v_cvt_pk_bf16_f32 v9, v114, v115
	s_add_i32 s13, s2, 7
	s_and_b32 s13, s13, 7
	s_mul_i32 s14, s13, 0x1100
	v_add_u32_e32 v10, s14, v58
	ds_write_b64 v10, v[8:9]
	s_waitcnt vmcnt(16)
	v_pk_mul_f32 v[116:117], v[198:199], v[116:117] op_sel_hi:[0,1]
	v_pk_mul_f32 v[118:119], v[198:199], v[118:119] op_sel_hi:[0,1]
	s_waitcnt vmcnt(15)
	v_mul_f32_e32 v6, v117, v133
	v_mul_f32_e32 v7, v119, v135
	v_fmac_f32_e32 v6, v116, v132
	v_fmac_f32_e32 v7, v118, v134
	s_and_b32 s13, s2, 15
	s_mul_i32 s14, s13, 0x104
	s_mul_i32 s15, s13, 0x110
	v_add_f32_e32 v6, v6, v7
	v_add_u32_e32 v125, s14, v59
	ds_write_b32 v125, v6
	v_cvt_pk_bf16_f32 v8, v132, v133
	v_cvt_pk_bf16_f32 v9, v134, v135
	v_add_u32_e32 v10, s15, v76
	s_mov_b64 exec, s[48:49]
	ds_write_b64 v10, v[8:9]
	s_mov_b64 exec, -1
	s_waitcnt vmcnt(14)
	v_mul_f32_e32 v11, v117, v137
	v_mul_f32_e32 v15, v119, v139
	v_fmac_f32_e32 v11, v116, v136
	v_fmac_f32_e32 v15, v118, v138
	s_add_i32 s13, s2, 1
	s_and_b32 s13, s13, 15
	s_mul_i32 s14, s13, 0x104
	s_mul_i32 s15, s13, 0x110
	v_add_f32_e32 v11, v11, v15
	v_add_u32_e32 v16, s14, v59
	ds_write_b32 v16, v11
	v_cvt_pk_bf16_f32 v12, v136, v137
	v_cvt_pk_bf16_f32 v13, v138, v139
	v_add_u32_e32 v14, s15, v76
	s_mov_b64 exec, s[48:49]
	ds_write_b64 v14, v[12:13]
	s_mov_b64 exec, -1
	s_waitcnt vmcnt(13)
	v_mul_f32_e32 v6, v117, v141
	v_mul_f32_e32 v7, v119, v143
	v_fmac_f32_e32 v6, v116, v140
	v_fmac_f32_e32 v7, v118, v142
	s_add_i32 s13, s2, 2
	s_and_b32 s13, s13, 15
	s_mul_i32 s14, s13, 0x104
	s_mul_i32 s15, s13, 0x110
	v_add_f32_e32 v6, v6, v7
	v_add_u32_e32 v125, s14, v59
	ds_write_b32 v125, v6
	v_cvt_pk_bf16_f32 v8, v140, v141
	v_cvt_pk_bf16_f32 v9, v142, v143
	v_add_u32_e32 v10, s15, v76
	s_mov_b64 exec, s[48:49]
	ds_write_b64 v10, v[8:9]
	s_mov_b64 exec, -1
	s_waitcnt vmcnt(12)
	v_mul_f32_e32 v11, v117, v145
	v_mul_f32_e32 v15, v119, v147
	v_fmac_f32_e32 v11, v116, v144
	v_fmac_f32_e32 v15, v118, v146
	s_add_i32 s13, s2, 3
	s_and_b32 s13, s13, 15
	s_mul_i32 s14, s13, 0x104
	s_mul_i32 s15, s13, 0x110
	v_add_f32_e32 v11, v11, v15
	v_add_u32_e32 v16, s14, v59
	ds_write_b32 v16, v11
	v_cvt_pk_bf16_f32 v12, v144, v145
	v_cvt_pk_bf16_f32 v13, v146, v147
	v_add_u32_e32 v14, s15, v76
	s_mov_b64 exec, s[48:49]
	ds_write_b64 v14, v[12:13]
	s_mov_b64 exec, -1
	s_waitcnt vmcnt(11)
	v_mul_f32_e32 v6, v117, v149
	v_mul_f32_e32 v7, v119, v151
	v_fmac_f32_e32 v6, v116, v148
	v_fmac_f32_e32 v7, v118, v150
	s_add_i32 s13, s2, 4
	s_and_b32 s13, s13, 15
	s_mul_i32 s14, s13, 0x104
	s_mul_i32 s15, s13, 0x110
	v_add_f32_e32 v6, v6, v7
	v_add_u32_e32 v125, s14, v59
	ds_write_b32 v125, v6
	v_cvt_pk_bf16_f32 v8, v148, v149
	v_cvt_pk_bf16_f32 v9, v150, v151
	v_add_u32_e32 v10, s15, v76
	s_mov_b64 exec, s[48:49]
	ds_write_b64 v10, v[8:9]
	s_mov_b64 exec, -1
	s_waitcnt vmcnt(10)
	v_mul_f32_e32 v11, v117, v153
	v_mul_f32_e32 v15, v119, v155
	v_fmac_f32_e32 v11, v116, v152
	v_fmac_f32_e32 v15, v118, v154
	s_add_i32 s13, s2, 5
	s_and_b32 s13, s13, 15
	s_mul_i32 s14, s13, 0x104
	s_mul_i32 s15, s13, 0x110
	v_add_f32_e32 v11, v11, v15
	v_add_u32_e32 v16, s14, v59
	ds_write_b32 v16, v11
	v_cvt_pk_bf16_f32 v12, v152, v153
	v_cvt_pk_bf16_f32 v13, v154, v155
	v_add_u32_e32 v14, s15, v76
	s_mov_b64 exec, s[48:49]
	ds_write_b64 v14, v[12:13]
	s_mov_b64 exec, -1
	s_waitcnt vmcnt(9)
	v_mul_f32_e32 v6, v117, v157
	v_mul_f32_e32 v7, v119, v159
	v_fmac_f32_e32 v6, v116, v156
	v_fmac_f32_e32 v7, v118, v158
	s_add_i32 s13, s2, 6
	s_and_b32 s13, s13, 15
	s_mul_i32 s14, s13, 0x104
	s_mul_i32 s15, s13, 0x110
	v_add_f32_e32 v6, v6, v7
	v_add_u32_e32 v125, s14, v59
	ds_write_b32 v125, v6
	v_cvt_pk_bf16_f32 v8, v156, v157
	v_cvt_pk_bf16_f32 v9, v158, v159
	v_add_u32_e32 v10, s15, v76
	s_mov_b64 exec, s[48:49]
	ds_write_b64 v10, v[8:9]
	s_mov_b64 exec, -1
	s_waitcnt vmcnt(8)
	v_mul_f32_e32 v11, v117, v161
	v_mul_f32_e32 v15, v119, v163
	v_fmac_f32_e32 v11, v116, v160
	v_fmac_f32_e32 v15, v118, v162
	s_add_i32 s13, s2, 7
	s_and_b32 s13, s13, 15
	s_mul_i32 s14, s13, 0x104
	s_mul_i32 s15, s13, 0x110
	v_add_f32_e32 v11, v11, v15
	v_add_u32_e32 v16, s14, v59
	ds_write_b32 v16, v11
	v_cvt_pk_bf16_f32 v12, v160, v161
	v_cvt_pk_bf16_f32 v13, v162, v163
	v_add_u32_e32 v14, s15, v76
	s_mov_b64 exec, s[48:49]
	ds_write_b64 v14, v[12:13]
	s_mov_b64 exec, -1
	s_waitcnt vmcnt(7)
	v_mul_f32_e32 v6, v117, v165
	v_mul_f32_e32 v7, v119, v167
	v_fmac_f32_e32 v6, v116, v164
	v_fmac_f32_e32 v7, v118, v166
	s_add_i32 s13, s2, 8
	s_and_b32 s13, s13, 15
	s_mul_i32 s14, s13, 0x104
	s_mul_i32 s15, s13, 0x110
	v_add_f32_e32 v6, v6, v7
	v_add_u32_e32 v125, s14, v59
	ds_write_b32 v125, v6
	v_cvt_pk_bf16_f32 v8, v164, v165
	v_cvt_pk_bf16_f32 v9, v166, v167
	v_add_u32_e32 v10, s15, v76
	s_mov_b64 exec, s[48:49]
	ds_write_b64 v10, v[8:9]
	s_mov_b64 exec, -1
	s_waitcnt vmcnt(6)
	v_mul_f32_e32 v11, v117, v169
	v_mul_f32_e32 v15, v119, v171
	v_fmac_f32_e32 v11, v116, v168
	v_fmac_f32_e32 v15, v118, v170
	s_add_i32 s13, s2, 9
	s_and_b32 s13, s13, 15
	s_mul_i32 s14, s13, 0x104
	s_mul_i32 s15, s13, 0x110
	v_add_f32_e32 v11, v11, v15
	v_add_u32_e32 v16, s14, v59
	ds_write_b32 v16, v11
	v_cvt_pk_bf16_f32 v12, v168, v169
	v_cvt_pk_bf16_f32 v13, v170, v171
	v_add_u32_e32 v14, s15, v76
	s_mov_b64 exec, s[48:49]
	ds_write_b64 v14, v[12:13]
	s_mov_b64 exec, -1
	s_waitcnt vmcnt(5)
	v_mul_f32_e32 v6, v117, v173
	v_mul_f32_e32 v7, v119, v175
	v_fmac_f32_e32 v6, v116, v172
	v_fmac_f32_e32 v7, v118, v174
	s_add_i32 s13, s2, 10
	s_and_b32 s13, s13, 15
	s_mul_i32 s14, s13, 0x104
	s_mul_i32 s15, s13, 0x110
	v_add_f32_e32 v6, v6, v7
	v_add_u32_e32 v125, s14, v59
	ds_write_b32 v125, v6
	v_cvt_pk_bf16_f32 v8, v172, v173
	v_cvt_pk_bf16_f32 v9, v174, v175
	v_add_u32_e32 v10, s15, v76
	s_mov_b64 exec, s[48:49]
	ds_write_b64 v10, v[8:9]
	s_mov_b64 exec, -1
	s_waitcnt vmcnt(4)
	v_mul_f32_e32 v11, v117, v177
	v_mul_f32_e32 v15, v119, v179
	v_fmac_f32_e32 v11, v116, v176
	v_fmac_f32_e32 v15, v118, v178
	s_add_i32 s13, s2, 11
	s_and_b32 s13, s13, 15
	s_mul_i32 s14, s13, 0x104
	s_mul_i32 s15, s13, 0x110
	v_add_f32_e32 v11, v11, v15
	v_add_u32_e32 v16, s14, v59
	ds_write_b32 v16, v11
	v_cvt_pk_bf16_f32 v12, v176, v177
	v_cvt_pk_bf16_f32 v13, v178, v179
	v_add_u32_e32 v14, s15, v76
	s_mov_b64 exec, s[48:49]
	ds_write_b64 v14, v[12:13]
	s_mov_b64 exec, -1
	s_waitcnt vmcnt(3)
	v_mul_f32_e32 v6, v117, v181
	v_mul_f32_e32 v7, v119, v183
	v_fmac_f32_e32 v6, v116, v180
	v_fmac_f32_e32 v7, v118, v182
	s_add_i32 s13, s2, 12
	s_and_b32 s13, s13, 15
	s_mul_i32 s14, s13, 0x104
	s_mul_i32 s15, s13, 0x110
	v_add_f32_e32 v6, v6, v7
	v_add_u32_e32 v125, s14, v59
	ds_write_b32 v125, v6
	v_cvt_pk_bf16_f32 v8, v180, v181
	v_cvt_pk_bf16_f32 v9, v182, v183
	v_add_u32_e32 v10, s15, v76
	s_mov_b64 exec, s[48:49]
	ds_write_b64 v10, v[8:9]
	s_mov_b64 exec, -1
	s_waitcnt vmcnt(2)
	v_mul_f32_e32 v11, v117, v185
	v_mul_f32_e32 v15, v119, v187
	v_fmac_f32_e32 v11, v116, v184
	v_fmac_f32_e32 v15, v118, v186
	s_add_i32 s13, s2, 13
	s_and_b32 s13, s13, 15
	s_mul_i32 s14, s13, 0x104
	s_mul_i32 s15, s13, 0x110
	v_add_f32_e32 v11, v11, v15
	v_add_u32_e32 v16, s14, v59
	ds_write_b32 v16, v11
	v_cvt_pk_bf16_f32 v12, v184, v185
	v_cvt_pk_bf16_f32 v13, v186, v187
	v_add_u32_e32 v14, s15, v76
	s_mov_b64 exec, s[48:49]
	ds_write_b64 v14, v[12:13]
	s_mov_b64 exec, -1
	s_waitcnt vmcnt(1)
	v_mul_f32_e32 v6, v117, v189
	v_mul_f32_e32 v7, v119, v191
	v_fmac_f32_e32 v6, v116, v188
	v_fmac_f32_e32 v7, v118, v190
	s_add_i32 s13, s2, 14
	s_and_b32 s13, s13, 15
	s_mul_i32 s14, s13, 0x104
	s_mul_i32 s15, s13, 0x110
	v_add_f32_e32 v6, v6, v7
	v_add_u32_e32 v125, s14, v59
	ds_write_b32 v125, v6
	v_cvt_pk_bf16_f32 v8, v188, v189
	v_cvt_pk_bf16_f32 v9, v190, v191
	v_add_u32_e32 v10, s15, v76
	s_mov_b64 exec, s[48:49]
	ds_write_b64 v10, v[8:9]
	s_mov_b64 exec, -1
	s_waitcnt vmcnt(0)
	v_mul_f32_e32 v11, v117, v193
	v_mul_f32_e32 v15, v119, v195
	v_fmac_f32_e32 v11, v116, v192
	v_fmac_f32_e32 v15, v118, v194
	s_add_i32 s13, s2, 15
	s_and_b32 s13, s13, 15
	s_mul_i32 s14, s13, 0x104
	s_mul_i32 s15, s13, 0x110
	v_add_f32_e32 v11, v11, v15
	v_add_u32_e32 v16, s14, v59
	ds_write_b32 v16, v11
	v_cvt_pk_bf16_f32 v12, v192, v193
	v_cvt_pk_bf16_f32 v13, v194, v195
	v_add_u32_e32 v14, s15, v76
	s_mov_b64 exec, s[48:49]
	ds_write_b64 v14, v[12:13]
	s_mov_b64 exec, -1
	s_waitcnt lgkmcnt(0)
	ds_read2_b32 v[60:61], v77 offset0:0 offset1:1
	ds_read2_b32 v[62:63], v77 offset0:2 offset1:3
	ds_read2_b32 v[64:65], v77 offset0:4 offset1:5
	ds_read2_b32 v[66:67], v77 offset0:6 offset1:7
	ds_read2_b32 v[68:69], v77 offset0:8 offset1:9
	ds_read2_b32 v[70:71], v77 offset0:10 offset1:11
	ds_read2_b32 v[72:73], v77 offset0:12 offset1:13
	ds_read2_b32 v[74:75], v77 offset0:14 offset1:15
	s_waitcnt lgkmcnt(0)
	v_add_f32_e32 v78, 0, v60
	v_add_f32_e32 v78, v78, v61
	v_add_f32_e32 v78, v78, v62
	v_add_f32_e32 v78, v78, v63
	v_add_f32_e32 v78, v78, v64
	v_add_f32_e32 v78, v78, v65
	v_add_f32_e32 v78, v78, v66
	v_add_f32_e32 v78, v78, v67
	v_add_f32_e32 v78, v78, v68
	v_add_f32_e32 v78, v78, v69
	v_add_f32_e32 v78, v78, v70
	v_add_f32_e32 v78, v78, v71
	v_add_f32_e32 v78, v78, v72
	v_add_f32_e32 v78, v78, v73
	v_add_f32_e32 v78, v78, v74
	v_add_f32_e32 v78, v78, v75
	s_nop 1
	v_add_f32_dpp v78, v78, v78 quad_perm:[1,0,3,2] row_mask:0xf bank_mask:0xf bound_ctrl:1
	s_nop 1
	v_add_f32_dpp v78, v78, v78 quad_perm:[2,3,0,1] row_mask:0xf bank_mask:0xf bound_ctrl:1
	v_lshlrev_b32_e32 v79, 4, v1
	ds_bpermute_b32 v78, v79, v78
	v_readfirstlane_b32 s78, v128
	s_cmp_lt_u32 s78, 4
	s_cbranch_scc0 .Lk_nomask
	s_add_i32 s79, s3, 12
	s_add_i32 s79, s79, s78
	s_lshl_b32 s80, s79, 12
	v_lshl_add_u32 v123, v126, 4, s80
	global_load_dwordx4 v[2:5], v123, s[34:35] nt
	global_load_dwordx4 v[6:9], v123, s[34:35] offset:1024 nt
	global_load_dwordx4 v[10:13], v123, s[34:35] offset:2048 nt
	global_load_dwordx4 v[14:17], v123, s[34:35] offset:3072 nt
.Lk_nomask:
	s_waitcnt lgkmcnt(0)
	s_barrier
	ds_read_b128 v[28:31], v53
	ds_read_b128 v[60:63], v56
	ds_read_b128 v[32:35], v53 offset:64
	ds_read_b128 v[64:67], v56 offset:64
	ds_read_b128 v[36:39], v53 offset:128
	ds_read_b128 v[68:71], v56 offset:128
	ds_read_b128 v[40:43], v53 offset:192
	ds_read_b128 v[72:75], v56 offset:192
	s_waitcnt lgkmcnt(6)
	v_mfma_f32_16x16x32_bf16 v[18:21], v[28:31], v[60:63], 0
	s_waitcnt lgkmcnt(4)
	v_mfma_f32_16x16x32_bf16 v[18:21], v[32:35], v[64:67], v[18:21]
	s_waitcnt lgkmcnt(2)
	v_mfma_f32_16x16x32_bf16 v[18:21], v[36:39], v[68:71], v[18:21]
	s_waitcnt lgkmcnt(0)
	v_mfma_f32_16x16x32_bf16 v[18:21], v[40:43], v[72:75], v[18:21]
	s_nop 7
	v_mul_f32_e32 v18, s44, v18
	v_mul_f32_e32 v19, s44, v19
	v_mul_f32_e32 v20, s44, v20
	v_mul_f32_e32 v21, s44, v21
	v_cvt_pk_bf16_f32 v18, v18, v18
	v_cvt_pk_bf16_f32 v19, v19, v19
	v_cvt_pk_bf16_f32 v20, v20, v20
	v_cvt_pk_bf16_f32 v21, v21, v21
	ds_write_b16 v55, v18
	ds_write_b16 v55, v19 offset:272
	ds_write_b16 v55, v20 offset:544
	ds_write_b16 v55, v21 offset:816
	s_waitcnt lgkmcnt(0)
	s_barrier
	ds_read_b128 v[28:31], v54
	ds_read_b128 v[60:63], v57
	ds_read_b128 v[32:35], v54 offset:64
	ds_read_b128 v[64:67], v57 offset:64
	ds_read_b128 v[36:39], v54 offset:128
	ds_read_b128 v[68:71], v57 offset:128
	ds_read_b128 v[40:43], v54 offset:192
	ds_read_b128 v[72:75], v57 offset:192
	s_waitcnt lgkmcnt(6)
	v_mfma_f32_16x16x32_bf16 v[18:21], v[28:31], v[60:63], 0
	s_waitcnt lgkmcnt(4)
	v_mfma_f32_16x16x32_bf16 v[18:21], v[32:35], v[64:67], v[18:21]
	s_waitcnt lgkmcnt(2)
	v_mfma_f32_16x16x32_bf16 v[18:21], v[36:39], v[68:71], v[18:21]
	s_waitcnt lgkmcnt(0)
	v_mfma_f32_16x16x32_bf16 v[18:21], v[40:43], v[72:75], v[18:21]
	s_nop 2
	v_mov_b32_e32 v28, v78
	s_load_dwordx2 s[4:5], s[0:1], 0x70
	v_lshl_or_b32 v30, v24, 2, s3
	v_ashrrev_i32_e32 v31, 31, v30
	v_mov_b32_e32 v107, 0
	s_waitcnt lgkmcnt(0)
	v_add_f32_e32 v34, v130, v28
	v_add_f32_e32 v35, v34, v18
	v_add_f32_e32 v28, v35, v35
	v_mul_f32_e32 v28, 0x3fb8aa3b, v28
	v_exp_f32_e32 v32, v28
	v_lshlrev_b64 v[28:29], 9, v[30:31]
	s_mov_b32 s8, 0x19200
	v_add3_u32 v37, v27, v25, s8
	v_add_f32_e32 v31, 1.0, v32
	v_rcp_f32_e32 v31, v31
	v_lshl_add_u64 v[32:33], s[4:5], 0, v[106:107]
	v_lshl_add_u64 v[28:29], v[32:33], 0, v[28:29]
	global_store_dword v[28:29], v35, off sc1
	v_fma_f32 v35, v31, -2.0, 1.0
	v_fma_f32 v28, -v35, v35, 1.0
	v_mul_f32_e32 v28, v129, v28
	v_add_f32_e32 v31, v34, v19
	v_cvt_pk_bf16_f32 v29, v28, s0
	v_mul_f32_e64 v27, v35, -v28
	v_add_f32_e32 v28, v31, v31
	v_mul_f32_e32 v28, 0x3fb8aa3b, v28
	v_exp_f32_e32 v38, v28
	v_cvt_pk_bf16_f32 v27, v27, s0
	ds_write_b16 v37, v27 offset:4352
	v_or_b32_e32 v28, 1, v30
	v_add_f32_e32 v27, 1.0, v38
	v_rcp_f32_e32 v27, v27
	ds_write_b16 v37, v29
	v_ashrrev_i32_e32 v29, 31, v28
	v_lshlrev_b64 v[28:29], 9, v[28:29]
	v_lshl_add_u64 v[28:29], v[32:33], 0, v[28:29]
	v_fma_f32 v27, v27, -2.0, 1.0
	global_store_dword v[28:29], v31, off sc1
	v_fma_f32 v28, -v27, v27, 1.0
	v_mul_f32_e32 v28, v129, v28
	v_cvt_pk_bf16_f32 v29, v28, s0
	v_add_f32_e32 v31, v34, v20
	ds_write_b16 v37, v29 offset:272
	v_add_f32_e32 v29, v31, v31
	v_mul_f32_e32 v29, 0x3fb8aa3b, v29
	v_exp_f32_e32 v38, v29
	v_mul_f32_e64 v28, v27, -v28
	v_cvt_pk_bf16_f32 v28, v28, s0
	ds_write_b16 v37, v28 offset:4624
	v_add_f32_e32 v38, 1.0, v38
	v_or_b32_e32 v28, 2, v30
	v_rcp_f32_e32 v38, v38
	v_ashrrev_i32_e32 v29, 31, v28
	v_lshlrev_b64 v[28:29], 9, v[28:29]
	v_lshl_add_u64 v[28:29], v[32:33], 0, v[28:29]
	global_store_dword v[28:29], v31, off sc1
	v_fma_f32 v28, v38, -2.0, 1.0
	v_fma_f32 v29, -v28, v28, 1.0
	v_mul_f32_e32 v29, v129, v29
	v_cvt_pk_bf16_f32 v31, v29, s0
	v_add_f32_e32 v34, v34, v21
	ds_write_b16 v37, v31 offset:544
	v_add_f32_e32 v31, v34, v34
	v_mul_f32_e32 v31, 0x3fb8aa3b, v31
	v_exp_f32_e32 v38, v31
	v_mul_f32_e64 v29, v28, -v29
	v_cvt_pk_bf16_f32 v29, v29, s0
	ds_write_b16 v37, v29 offset:4896
	v_add_f32_e32 v29, 1.0, v38
	v_rcp_f32_e32 v29, v29
	v_or_b32_e32 v30, 3, v30
	v_ashrrev_i32_e32 v31, 31, v30
	v_lshlrev_b64 v[30:31], 9, v[30:31]
	v_lshl_add_u64 v[30:31], v[32:33], 0, v[30:31]
	v_fma_f32 v29, v29, -2.0, 1.0
	global_store_dword v[30:31], v34, off sc1
	v_fma_f32 v30, -v29, v29, 1.0
	v_mul_f32_e32 v30, v129, v30
	v_cvt_pk_bf16_f32 v31, v30, s0
	v_mul_f32_e64 v30, v29, -v30
	v_cvt_pk_bf16_f32 v30, v30, s0
	ds_write_b16 v37, v30 offset:5168
	v_mov_b32_e32 v30, 0x1d800
	v_mul_f32_e32 v36, v129, v35
	v_lshl_or_b32 v32, v128, 6, v30
	v_mov_b32_e32 v30, v107
	ds_write_b16 v37, v31 offset:816
	v_mov_b32_e32 v31, 0
	v_mov_b32_dpp v30, v36 quad_perm:[1,0,3,2] row_mask:0xf bank_mask:0xf
	v_fmac_f32_e32 v30, v129, v35
	v_cmp_eq_u32_e32 vcc, 0, v1
	v_add_u32_e32 v26, v32, v26
	v_add_f32_dpp v30, v30, v30 quad_perm:[2,3,0,1] row_mask:0xf bank_mask:0xf bound_ctrl:1
	s_nop 1
	v_add_f32_dpp v30, v30, v30 row_half_mirror row_mask:0xf bank_mask:0xf bound_ctrl:1
	s_nop 1
	v_mov_b32_dpp v31, v30 row_mirror row_mask:0xf bank_mask:0xf
	s_and_saveexec_b64 s[4:5], vcc
	v_add_f32_e32 v30, v30, v31
	ds_write_b32 v26, v30
	s_or_b64 exec, exec, s[4:5]
	v_mul_f32_e32 v30, v129, v27
	v_mov_b32_e32 v31, 0
	s_nop 1
	v_mov_b32_dpp v31, v30 quad_perm:[1,0,3,2] row_mask:0xf bank_mask:0xf
	v_fmac_f32_e32 v31, v129, v27
	s_nop 1
	v_add_f32_dpp v27, v31, v31 quad_perm:[2,3,0,1] row_mask:0xf bank_mask:0xf bound_ctrl:1
	s_nop 1
	v_add_f32_dpp v27, v27, v27 row_half_mirror row_mask:0xf bank_mask:0xf bound_ctrl:1
	s_nop 1
	v_mov_b32_dpp v107, v27 row_mirror row_mask:0xf bank_mask:0xf
	s_and_saveexec_b64 s[4:5], vcc
	v_add_f32_e32 v27, v27, v107
	ds_write_b32 v26, v27 offset:4
	s_or_b64 exec, exec, s[4:5]
	v_mul_f32_e32 v30, v129, v28
	v_mov_b32_e32 v31, 0
	v_mov_b32_e32 v27, 0
	s_nop 0
	v_mov_b32_dpp v31, v30 quad_perm:[1,0,3,2] row_mask:0xf bank_mask:0xf
	v_fmac_f32_e32 v31, v129, v28
	v_mov_b32_e32 v30, 0
	s_nop 0
	v_add_f32_dpp v28, v31, v31 quad_perm:[2,3,0,1] row_mask:0xf bank_mask:0xf bound_ctrl:1
	s_nop 1
	v_add_f32_dpp v28, v28, v28 row_half_mirror row_mask:0xf bank_mask:0xf bound_ctrl:1
	s_nop 1
	v_mov_b32_dpp v30, v28 row_mirror row_mask:0xf bank_mask:0xf
	s_and_saveexec_b64 s[4:5], vcc
	v_add_f32_e32 v28, v28, v30
	ds_write_b32 v26, v28 offset:8
	s_or_b64 exec, exec, s[4:5]
	v_mul_f32_e32 v28, v129, v29
	v_mov_b32_e32 v30, 0
	s_nop 1
	v_mov_b32_dpp v30, v28 quad_perm:[1,0,3,2] row_mask:0xf bank_mask:0xf
	v_fmac_f32_e32 v30, v129, v29
	s_nop 1
	v_add_f32_dpp v28, v30, v30 quad_perm:[2,3,0,1] row_mask:0xf bank_mask:0xf bound_ctrl:1
	s_nop 1
	v_add_f32_dpp v28, v28, v28 row_half_mirror row_mask:0xf bank_mask:0xf bound_ctrl:1
	s_nop 1
	v_mov_b32_dpp v27, v28 row_mirror row_mask:0xf bank_mask:0xf
	s_and_saveexec_b64 s[4:5], vcc
	v_add_f32_e32 v27, v28, v27
	ds_write_b32 v26, v27 offset:12
	s_or_b64 exec, exec, s[4:5]
	s_mov_b64 s[4:5], 0
	s_branch .LBB0_28
.Lp_q:
	v_lshrrev_b32_e32 v122, 5, v0
	v_lshlrev_b32_e32 v122, 10, v122
	v_and_b32_e32 v125, 31, v0
	v_lshl_add_u32 v122, v125, 4, v122
	s_and_b32 s13, s2, 7
	s_lshl_b32 s14, s13, 14
	v_add_u32_e32 v125, s14, v122
	global_load_dwordx4 v[132:135], v125, s[28:29]
	s_add_i32 s13, s2, 1
	s_and_b32 s13, s13, 7
	s_lshl_b32 s14, s13, 14
	v_add_u32_e32 v125, s14, v122
	global_load_dwordx4 v[136:139], v125, s[28:29]
	s_add_i32 s13, s2, 2
	s_and_b32 s13, s13, 7
	s_lshl_b32 s14, s13, 14
	v_add_u32_e32 v125, s14, v122
	global_load_dwordx4 v[140:143], v125, s[28:29]
	s_add_i32 s13, s2, 3
	s_and_b32 s13, s13, 7
	s_lshl_b32 s14, s13, 14
	v_add_u32_e32 v125, s14, v122
	global_load_dwordx4 v[144:147], v125, s[28:29]
	s_add_i32 s13, s2, 4
	s_and_b32 s13, s13, 7
	s_lshl_b32 s14, s13, 14
	v_add_u32_e32 v125, s14, v122
	global_load_dwordx4 v[148:151], v125, s[28:29]
	s_add_i32 s13, s2, 5
	s_and_b32 s13, s13, 7
	s_lshl_b32 s14, s13, 14
	v_add_u32_e32 v125, s14, v122
	global_load_dwordx4 v[152:155], v125, s[28:29]
	s_add_i32 s13, s2, 6
	s_and_b32 s13, s13, 7
	s_lshl_b32 s14, s13, 14
	v_add_u32_e32 v125, s14, v122
	global_load_dwordx4 v[156:159], v125, s[28:29]
	s_add_i32 s13, s2, 7
	s_and_b32 s13, s13, 7
	s_lshl_b32 s14, s13, 14
	v_add_u32_e32 v125, s14, v122
	global_load_dwordx4 v[160:163], v125, s[28:29]
	s_waitcnt vmcnt(18)
	v_cvt_pk_bf16_f32 v12, v2, v3
	v_cvt_pk_bf16_f32 v13, v4, v5
	ds_write_b64 v124, v[12:13]
	s_waitcnt vmcnt(17)
	v_cvt_pk_bf16_f32 v6, v80, v81
	v_cvt_pk_bf16_f32 v7, v82, v83
	s_and_b32 s13, s2, 7
	s_mul_i32 s14, s13, 0x1100
	v_add_u32_e32 v125, s14, v58
	ds_write_b64 v125, v[6:7]
	s_waitcnt vmcnt(16)
	v_cvt_pk_bf16_f32 v8, v84, v85
	v_cvt_pk_bf16_f32 v9, v86, v87
	s_add_i32 s13, s2, 1
	s_and_b32 s13, s13, 7
	s_mul_i32 s14, s13, 0x1100
	v_add_u32_e32 v10, s14, v58
	ds_write_b64 v10, v[8:9]
	s_waitcnt vmcnt(15)
	v_cvt_pk_bf16_f32 v6, v88, v89
	v_cvt_pk_bf16_f32 v7, v90, v91
	s_add_i32 s13, s2, 2
	s_and_b32 s13, s13, 7
	s_mul_i32 s14, s13, 0x1100
	v_add_u32_e32 v125, s14, v58
	ds_write_b64 v125, v[6:7]
	s_waitcnt vmcnt(14)
	v_cvt_pk_bf16_f32 v8, v92, v93
	v_cvt_pk_bf16_f32 v9, v94, v95
	s_add_i32 s13, s2, 3
	s_and_b32 s13, s13, 7
	s_mul_i32 s14, s13, 0x1100
	v_add_u32_e32 v10, s14, v58
	ds_write_b64 v10, v[8:9]
	s_waitcnt vmcnt(13)
	v_cvt_pk_bf16_f32 v6, v96, v97
	v_cvt_pk_bf16_f32 v7, v98, v99
	s_add_i32 s13, s2, 4
	s_and_b32 s13, s13, 7
	s_mul_i32 s14, s13, 0x1100
	v_add_u32_e32 v125, s14, v58
	ds_write_b64 v125, v[6:7]
	s_waitcnt vmcnt(12)
	v_cvt_pk_bf16_f32 v8, v100, v101
	v_cvt_pk_bf16_f32 v9, v102, v103
	s_add_i32 s13, s2, 5
	s_and_b32 s13, s13, 7
	s_mul_i32 s14, s13, 0x1100
	v_add_u32_e32 v10, s14, v58
	ds_write_b64 v10, v[8:9]
	s_waitcnt vmcnt(11)
	v_cvt_pk_bf16_f32 v6, v108, v109
	v_cvt_pk_bf16_f32 v7, v110, v111
	s_add_i32 s13, s2, 6
	s_and_b32 s13, s13, 7
	s_mul_i32 s14, s13, 0x1100
	v_add_u32_e32 v125, s14, v58
	ds_write_b64 v125, v[6:7]
	s_waitcnt vmcnt(10)
	v_cvt_pk_bf16_f32 v8, v112, v113
	v_cvt_pk_bf16_f32 v9, v114, v115
	s_add_i32 s13, s2, 7
	s_and_b32 s13, s13, 7
	s_mul_i32 s14, s13, 0x1100
	v_add_u32_e32 v10, s14, v58
	ds_write_b64 v10, v[8:9]
	s_waitcnt vmcnt(7)
	v_cvt_pk_bf16_f32 v6, v132, v133
	v_cvt_pk_bf16_f32 v7, v134, v135
	s_and_b32 s13, s2, 7
	s_mul_i32 s14, s13, 0x1100
	s_add_i32 s14, s14, 34816
	v_add_u32_e32 v125, s14, v58
	ds_write_b64 v125, v[6:7]
	s_waitcnt vmcnt(6)
	v_cvt_pk_bf16_f32 v8, v136, v137
	v_cvt_pk_bf16_f32 v9, v138, v139
	s_add_i32 s13, s2, 1
	s_and_b32 s13, s13, 7
	s_mul_i32 s14, s13, 0x1100
	s_add_i32 s14, s14, 34816
	v_add_u32_e32 v10, s14, v58
	ds_write_b64 v10, v[8:9]
	s_waitcnt vmcnt(5)
	v_cvt_pk_bf16_f32 v6, v140, v141
	v_cvt_pk_bf16_f32 v7, v142, v143
	s_add_i32 s13, s2, 2
	s_and_b32 s13, s13, 7
	s_mul_i32 s14, s13, 0x1100
	s_add_i32 s14, s14, 34816
	v_add_u32_e32 v125, s14, v58
	ds_write_b64 v125, v[6:7]
	s_waitcnt vmcnt(4)
	v_cvt_pk_bf16_f32 v8, v144, v145
	v_cvt_pk_bf16_f32 v9, v146, v147
	s_add_i32 s13, s2, 3
	s_and_b32 s13, s13, 7
	s_mul_i32 s14, s13, 0x1100
	s_add_i32 s14, s14, 34816
	v_add_u32_e32 v10, s14, v58
	ds_write_b64 v10, v[8:9]
	s_waitcnt vmcnt(3)
	v_cvt_pk_bf16_f32 v6, v148, v149
	v_cvt_pk_bf16_f32 v7, v150, v151
	s_add_i32 s13, s2, 4
	s_and_b32 s13, s13, 7
	s_mul_i32 s14, s13, 0x1100
	s_add_i32 s14, s14, 34816
	v_add_u32_e32 v125, s14, v58
	ds_write_b64 v125, v[6:7]
	s_waitcnt vmcnt(2)
	v_cvt_pk_bf16_f32 v8, v152, v153
	v_cvt_pk_bf16_f32 v9, v154, v155
	s_add_i32 s13, s2, 5
	s_and_b32 s13, s13, 7
	s_mul_i32 s14, s13, 0x1100
	s_add_i32 s14, s14, 34816
	v_add_u32_e32 v10, s14, v58
	ds_write_b64 v10, v[8:9]
	s_waitcnt vmcnt(1)
	v_cvt_pk_bf16_f32 v6, v156, v157
	v_cvt_pk_bf16_f32 v7, v158, v159
	s_add_i32 s13, s2, 6
	s_and_b32 s13, s13, 7
	s_mul_i32 s14, s13, 0x1100
	s_add_i32 s14, s14, 34816
	v_add_u32_e32 v125, s14, v58
	ds_write_b64 v125, v[6:7]
	s_waitcnt vmcnt(0)
	v_cvt_pk_bf16_f32 v8, v160, v161
	v_cvt_pk_bf16_f32 v9, v162, v163
	s_add_i32 s13, s2, 7
	s_and_b32 s13, s13, 7
	s_mul_i32 s14, s13, 0x1100
	s_add_i32 s14, s14, 34816
	v_add_u32_e32 v10, s14, v58
	ds_write_b64 v10, v[8:9]
	v_readfirstlane_b32 s78, v128
	s_lshl_b32 s80, s78, 1
	s_add_i32 s81, s78, 4
	s_cmp_lt_u32 s78, 4
	s_cselect_b32 s79, s80, s81
	s_add_i32 s79, s79, s12
	s_lshl_b32 s80, s79, 12
	v_lshl_add_u32 v123, v126, 4, s80
	global_load_dwordx4 v[164:167], v123, s[34:35] nt
	global_load_dwordx4 v[168:171], v123, s[34:35] offset:1024 nt
	global_load_dwordx4 v[172:175], v123, s[34:35] offset:2048 nt
	global_load_dwordx4 v[176:179], v123, s[34:35] offset:3072 nt
	s_cmp_lt_u32 s78, 4
	s_cbranch_scc0 .Lq_norowb
	v_add_u32_e32 v125, 0x1000, v123
	global_load_dwordx4 v[180:183], v125, s[34:35] nt
	global_load_dwordx4 v[184:187], v125, s[34:35] offset:1024 nt
	global_load_dwordx4 v[188:191], v125, s[34:35] offset:2048 nt
	global_load_dwordx4 v[192:195], v125, s[34:35] offset:3072 nt
.Lq_norowb:
	s_waitcnt lgkmcnt(0)
	s_barrier
	ds_read_b128 v[28:31], v53
	ds_read_b128 v[60:63], v56
	ds_read_b128 v[32:35], v53 offset:64
	ds_read_b128 v[64:67], v56 offset:64
	ds_read_b128 v[36:39], v53 offset:128
	ds_read_b128 v[68:71], v56 offset:128
	ds_read_b128 v[40:43], v53 offset:192
	ds_read_b128 v[72:75], v56 offset:192
	s_waitcnt lgkmcnt(6)
	v_mfma_f32_16x16x32_bf16 v[18:21], v[28:31], v[60:63], 0
	s_waitcnt lgkmcnt(4)
	v_mfma_f32_16x16x32_bf16 v[18:21], v[32:35], v[64:67], v[18:21]
	s_waitcnt lgkmcnt(2)
	v_mfma_f32_16x16x32_bf16 v[18:21], v[36:39], v[68:71], v[18:21]
	s_waitcnt lgkmcnt(0)
	v_mfma_f32_16x16x32_bf16 v[18:21], v[40:43], v[72:75], v[18:21]
	s_nop 7
	v_mul_f32_e32 v18, s44, v18
	v_mul_f32_e32 v19, s44, v19
	v_mul_f32_e32 v20, s44, v20
	v_mul_f32_e32 v21, s44, v21
	v_cvt_pk_bf16_f32 v18, v18, v18
	v_cvt_pk_bf16_f32 v19, v19, v19
	v_cvt_pk_bf16_f32 v20, v20, v20
	v_cvt_pk_bf16_f32 v21, v21, v21
	ds_write_b16 v55, v18
	ds_write_b16 v55, v19 offset:272
	ds_write_b16 v55, v20 offset:544
	ds_write_b16 v55, v21 offset:816
	s_waitcnt lgkmcnt(0)
	s_barrier
	ds_read_b128 v[28:31], v54
	ds_read_b128 v[60:63], v57
	ds_read_b128 v[32:35], v54 offset:64
	ds_read_b128 v[64:67], v57 offset:64
	ds_read_b128 v[36:39], v54 offset:128
	ds_read_b128 v[68:71], v57 offset:128
	ds_read_b128 v[40:43], v54 offset:192
	ds_read_b128 v[72:75], v57 offset:192
	s_waitcnt lgkmcnt(6)
	v_mfma_f32_16x16x32_bf16 v[18:21], v[28:31], v[60:63], 0
	s_waitcnt lgkmcnt(4)
	v_mfma_f32_16x16x32_bf16 v[18:21], v[32:35], v[64:67], v[18:21]
	s_waitcnt lgkmcnt(2)
	v_mfma_f32_16x16x32_bf16 v[18:21], v[36:39], v[68:71], v[18:21]
	s_waitcnt lgkmcnt(0)
	v_mfma_f32_16x16x32_bf16 v[18:21], v[40:43], v[72:75], v[18:21]
	s_load_dwordx2 s[4:5], s[0:1], 0x68
	v_lshl_or_b32 v26, v24, 2, s12
	v_mov_b32_e32 v107, 0
	v_ashrrev_i32_e32 v27, 31, v26
	v_lshlrev_b64 v[28:29], 9, v[26:27]
	s_waitcnt lgkmcnt(0)
	v_lshl_add_u64 v[30:31], s[4:5], 0, v[106:107]
	v_lshl_add_u64 v[28:29], v[30:31], 0, v[28:29]
	v_mul_u32_u24_e32 v24, 0x440, v24
	s_mov_b32 s4, 0x19200
	global_store_dword v[28:29], v18, off sc1
	v_add3_u32 v28, v24, v25, s4
	v_mul_f32_e32 v24, v18, v18
	v_cvt_pk_bf16_f32 v27, v18, s0
	v_cvt_pk_bf16_f32 v24, v24, s0
	ds_write_b16 v28, v27
	ds_write_b16 v28, v24 offset:4352
	v_max3_f32 v27, |v18|, 0, |v19|
	v_or_b32_e32 v24, 1, v26
	v_cvt_pk_bf16_f32 v18, v19, s0
	v_ashrrev_i32_e32 v25, 31, v24
	ds_write_b16 v28, v18 offset:272
	v_mul_f32_e32 v18, v19, v19
	v_lshlrev_b64 v[24:25], 9, v[24:25]
	v_cvt_pk_bf16_f32 v18, v18, s0
	v_lshl_add_u64 v[24:25], v[30:31], 0, v[24:25]
	ds_write_b16 v28, v18 offset:4624
	v_or_b32_e32 v18, 2, v26
	global_store_dword v[24:25], v19, off sc1
	v_ashrrev_i32_e32 v19, 31, v18
	v_lshlrev_b64 v[18:19], 9, v[18:19]
	v_lshl_add_u64 v[18:19], v[30:31], 0, v[18:19]
	global_store_dword v[18:19], v20, off sc1
	v_cvt_pk_bf16_f32 v18, v20, s0
	ds_write_b16 v28, v18 offset:544
	v_mul_f32_e32 v18, v20, v20
	v_cvt_pk_bf16_f32 v18, v18, s0
	ds_write_b16 v28, v18 offset:4896
	v_or_b32_e32 v18, 3, v26
	v_ashrrev_i32_e32 v19, 31, v18
	v_lshlrev_b64 v[18:19], 9, v[18:19]
	v_lshl_add_u64 v[18:19], v[30:31], 0, v[18:19]
	global_store_dword v[18:19], v21, off sc1
	v_cvt_pk_bf16_f32 v18, v21, s0
	ds_write_b16 v28, v18 offset:816
	v_mul_f32_e32 v18, v21, v21
	v_cvt_pk_bf16_f32 v18, v18, s0
	v_max3_f32 v20, v27, |v20|, |v21|
	ds_write_b16 v28, v18 offset:5168
	v_mov_b32_e32 v18, v107
	v_mov_b32_e32 v19, v107
	v_cmp_eq_u32_e32 vcc, 0, v126
	v_mov_b32_dpp v18, v20 quad_perm:[1,0,3,2] row_mask:0xf bank_mask:0xf
	v_max_f32_e32 v18, v18, v18
	v_max_f32_e32 v18, v20, v18
	s_nop 1
	v_mov_b32_dpp v19, v18 quad_perm:[2,3,0,1] row_mask:0xf bank_mask:0xf
	v_max_f32_e32 v19, v19, v19
	v_max_f32_e32 v18, v18, v19
	v_mov_b32_e32 v19, v107
	s_nop 1
	v_mov_b32_dpp v19, v18 row_half_mirror row_mask:0xf bank_mask:0xf
	v_max_f32_e32 v19, v19, v19
	v_max_f32_e32 v18, v18, v19
	v_mov_b32_e32 v19, v107
	s_nop 1
	v_mov_b32_dpp v19, v18 row_mirror row_mask:0xf bank_mask:0xf
	v_max_f32_e32 v19, v19, v19
	v_max_f32_e32 v18, v18, v19
	s_nop 0
	v_readlane_b32 s8, v18, 0
	v_readlane_b32 s9, v18, 16
	v_readlane_b32 s10, v18, 32
	v_readlane_b32 s11, v18, 48
	v_and_b32_e32 v18, 0x7fffffff, v129
	s_nop 1
	v_add_f32_dpp v18, v18, |v129| quad_perm:[1,0,3,2] row_mask:0xf bank_mask:0xf bound_ctrl:1
	s_nop 1
	v_add_f32_dpp v18, v18, v18 quad_perm:[2,3,0,1] row_mask:0xf bank_mask:0xf bound_ctrl:1
	s_nop 1
	v_add_f32_dpp v18, v18, v18 row_half_mirror row_mask:0xf bank_mask:0xf bound_ctrl:1
	s_nop 1
	v_mov_b32_dpp v107, v18 row_mirror row_mask:0xf bank_mask:0xf
	s_and_saveexec_b64 s[4:5], vcc
	s_cbranch_execz .LBB0_27
	v_mov_b32_e32 v19, 0x1d800
	v_lshl_or_b32 v20, v128, 6, v19
	v_add_f32_e32 v19, v18, v107
	v_max_f32_e64 v18, s11, s11
	v_max_f32_e64 v21, s10, s10
	v_max_f32_e32 v18, v21, v18
	v_mov_b32_e32 v21, s9
	v_max3_f32 v18, s8, v21, v18
	ds_write_b64 v20, v[18:19]

.LBB0_40:
	s_cmpk_gt_i32 s2, 0x7f
	s_cbranch_scc1 .Lk_pack
	s_cmp_lt_u32 s78, 4
	s_cbranch_scc0 .Lq_packa
	s_waitcnt vmcnt(9)
	v_mov_b32_e32 v44, 0
	v_cmp_ne_u32_e64 s[46:47], 0, v179
	v_cmp_ne_u32_e64 s[48:49], 0, v178
	v_cmp_ne_u32_e64 s[50:51], 0, v177
	v_cmp_ne_u32_e64 s[52:53], 0, v176
	v_addc_co_u32_e64 v44, s[54:55], v44, v44, s[46:47]
	v_addc_co_u32_e64 v44, s[54:55], v44, v44, s[48:49]
	v_addc_co_u32_e64 v44, s[54:55], v44, v44, s[50:51]
	v_addc_co_u32_e64 v44, s[54:55], v44, v44, s[52:53]
	v_cmp_ne_u32_e64 s[46:47], 0, v175
	v_cmp_ne_u32_e64 s[48:49], 0, v174
	v_cmp_ne_u32_e64 s[50:51], 0, v173
	v_cmp_ne_u32_e64 s[52:53], 0, v172
	v_addc_co_u32_e64 v44, s[54:55], v44, v44, s[46:47]
	v_addc_co_u32_e64 v44, s[54:55], v44, v44, s[48:49]
	v_addc_co_u32_e64 v44, s[54:55], v44, v44, s[50:51]
	v_addc_co_u32_e64 v44, s[54:55], v44, v44, s[52:53]
	v_cmp_ne_u32_e64 s[46:47], 0, v171
	v_cmp_ne_u32_e64 s[48:49], 0, v170
	v_cmp_ne_u32_e64 s[50:51], 0, v169
	v_cmp_ne_u32_e64 s[52:53], 0, v168
	v_addc_co_u32_e64 v44, s[54:55], v44, v44, s[46:47]
	v_addc_co_u32_e64 v44, s[54:55], v44, v44, s[48:49]
	v_addc_co_u32_e64 v44, s[54:55], v44, v44, s[50:51]
	v_addc_co_u32_e64 v44, s[54:55], v44, v44, s[52:53]
	v_cmp_ne_u32_e64 s[46:47], 0, v167
	v_cmp_ne_u32_e64 s[48:49], 0, v166
	v_cmp_ne_u32_e64 s[50:51], 0, v165
	v_cmp_ne_u32_e64 s[52:53], 0, v164
	v_addc_co_u32_e64 v44, s[54:55], v44, v44, s[46:47]
	v_addc_co_u32_e64 v44, s[54:55], v44, v44, s[48:49]
	v_addc_co_u32_e64 v44, s[54:55], v44, v44, s[50:51]
	v_addc_co_u32_e64 v44, s[54:55], v44, v44, s[52:53]
	s_waitcnt vmcnt(5)
	v_mov_b32_e32 v45, 0
	v_cmp_ne_u32_e64 s[46:47], 0, v195
	v_cmp_ne_u32_e64 s[48:49], 0, v194
	v_cmp_ne_u32_e64 s[50:51], 0, v193
	v_cmp_ne_u32_e64 s[52:53], 0, v192
	v_addc_co_u32_e64 v45, s[54:55], v45, v45, s[46:47]
	v_addc_co_u32_e64 v45, s[54:55], v45, v45, s[48:49]
	v_addc_co_u32_e64 v45, s[54:55], v45, v45, s[50:51]
	v_addc_co_u32_e64 v45, s[54:55], v45, v45, s[52:53]
	v_cmp_ne_u32_e64 s[46:47], 0, v191
	v_cmp_ne_u32_e64 s[48:49], 0, v190
	v_cmp_ne_u32_e64 s[50:51], 0, v189
	v_cmp_ne_u32_e64 s[52:53], 0, v188
	v_addc_co_u32_e64 v45, s[54:55], v45, v45, s[46:47]
	v_addc_co_u32_e64 v45, s[54:55], v45, v45, s[48:49]
	v_addc_co_u32_e64 v45, s[54:55], v45, v45, s[50:51]
	v_addc_co_u32_e64 v45, s[54:55], v45, v45, s[52:53]
	v_cmp_ne_u32_e64 s[46:47], 0, v187
	v_cmp_ne_u32_e64 s[48:49], 0, v186
	v_cmp_ne_u32_e64 s[50:51], 0, v185
	v_cmp_ne_u32_e64 s[52:53], 0, v184
	v_addc_co_u32_e64 v45, s[54:55], v45, v45, s[46:47]
	v_addc_co_u32_e64 v45, s[54:55], v45, v45, s[48:49]
	v_addc_co_u32_e64 v45, s[54:55], v45, v45, s[50:51]
	v_addc_co_u32_e64 v45, s[54:55], v45, v45, s[52:53]
	v_cmp_ne_u32_e64 s[46:47], 0, v183
	v_cmp_ne_u32_e64 s[48:49], 0, v182
	v_cmp_ne_u32_e64 s[50:51], 0, v181
	v_cmp_ne_u32_e64 s[52:53], 0, v180
	v_addc_co_u32_e64 v45, s[54:55], v45, v45, s[46:47]
	v_addc_co_u32_e64 v45, s[54:55], v45, v45, s[48:49]
	v_addc_co_u32_e64 v45, s[54:55], v45, v45, s[50:51]
	v_addc_co_u32_e64 v45, s[54:55], v45, v45, s[52:53]
	s_lshl_b32 s80, s79, 7
	v_lshl_add_u32 v46, v126, 1, s80
	global_store_short v46, v44, s[36:37] sc1
	global_store_short v46, v45, s[36:37] offset:128 sc1
	s_endpgm
.Lq_packa:
	s_waitcnt vmcnt(5)
	v_mov_b32_e32 v44, 0
	v_cmp_ne_u32_e64 s[46:47], 0, v179
	v_cmp_ne_u32_e64 s[48:49], 0, v178
	v_cmp_ne_u32_e64 s[50:51], 0, v177
	v_cmp_ne_u32_e64 s[52:53], 0, v176
	v_addc_co_u32_e64 v44, s[54:55], v44, v44, s[46:47]
	v_addc_co_u32_e64 v44, s[54:55], v44, v44, s[48:49]
	v_addc_co_u32_e64 v44, s[54:55], v44, v44, s[50:51]
	v_addc_co_u32_e64 v44, s[54:55], v44, v44, s[52:53]
	v_cmp_ne_u32_e64 s[46:47], 0, v175
	v_cmp_ne_u32_e64 s[48:49], 0, v174
	v_cmp_ne_u32_e64 s[50:51], 0, v173
	v_cmp_ne_u32_e64 s[52:53], 0, v172
	v_addc_co_u32_e64 v44, s[54:55], v44, v44, s[46:47]
	v_addc_co_u32_e64 v44, s[54:55], v44, v44, s[48:49]
	v_addc_co_u32_e64 v44, s[54:55], v44, v44, s[50:51]
	v_addc_co_u32_e64 v44, s[54:55], v44, v44, s[52:53]
	v_cmp_ne_u32_e64 s[46:47], 0, v171
	v_cmp_ne_u32_e64 s[48:49], 0, v170
	v_cmp_ne_u32_e64 s[50:51], 0, v169
	v_cmp_ne_u32_e64 s[52:53], 0, v168
	v_addc_co_u32_e64 v44, s[54:55], v44, v44, s[46:47]
	v_addc_co_u32_e64 v44, s[54:55], v44, v44, s[48:49]
	v_addc_co_u32_e64 v44, s[54:55], v44, v44, s[50:51]
	v_addc_co_u32_e64 v44, s[54:55], v44, v44, s[52:53]
	v_cmp_ne_u32_e64 s[46:47], 0, v167
	v_cmp_ne_u32_e64 s[48:49], 0, v166
	v_cmp_ne_u32_e64 s[50:51], 0, v165
	v_cmp_ne_u32_e64 s[52:53], 0, v164
	v_addc_co_u32_e64 v44, s[54:55], v44, v44, s[46:47]
	v_addc_co_u32_e64 v44, s[54:55], v44, v44, s[48:49]
	v_addc_co_u32_e64 v44, s[54:55], v44, v44, s[50:51]
	v_addc_co_u32_e64 v44, s[54:55], v44, v44, s[52:53]
	s_lshl_b32 s80, s79, 7
	v_lshl_add_u32 v46, v126, 1, s80
	global_store_short v46, v44, s[36:37] sc1
	s_endpgm
.Lk_pack:
	s_cmp_lt_u32 s78, 4
	s_cbranch_scc0 .Lp_end
	s_waitcnt vmcnt(5)
	v_mov_b32_e32 v44, 0
	v_cmp_ne_u32_e64 s[46:47], 0, v17
	v_cmp_ne_u32_e64 s[48:49], 0, v16
	v_cmp_ne_u32_e64 s[50:51], 0, v15
	v_cmp_ne_u32_e64 s[52:53], 0, v14
	v_addc_co_u32_e64 v44, s[54:55], v44, v44, s[46:47]
	v_addc_co_u32_e64 v44, s[54:55], v44, v44, s[48:49]
	v_addc_co_u32_e64 v44, s[54:55], v44, v44, s[50:51]
	v_addc_co_u32_e64 v44, s[54:55], v44, v44, s[52:53]
	v_cmp_ne_u32_e64 s[46:47], 0, v13
	v_cmp_ne_u32_e64 s[48:49], 0, v12
	v_cmp_ne_u32_e64 s[50:51], 0, v11
	v_cmp_ne_u32_e64 s[52:53], 0, v10
	v_addc_co_u32_e64 v44, s[54:55], v44, v44, s[46:47]
	v_addc_co_u32_e64 v44, s[54:55], v44, v44, s[48:49]
	v_addc_co_u32_e64 v44, s[54:55], v44, v44, s[50:51]
	v_addc_co_u32_e64 v44, s[54:55], v44, v44, s[52:53]
	v_cmp_ne_u32_e64 s[46:47], 0, v9
	v_cmp_ne_u32_e64 s[48:49], 0, v8
	v_cmp_ne_u32_e64 s[50:51], 0, v7
	v_cmp_ne_u32_e64 s[52:53], 0, v6
	v_addc_co_u32_e64 v44, s[54:55], v44, v44, s[46:47]
	v_addc_co_u32_e64 v44, s[54:55], v44, v44, s[48:49]
	v_addc_co_u32_e64 v44, s[54:55], v44, v44, s[50:51]
	v_addc_co_u32_e64 v44, s[54:55], v44, v44, s[52:53]
	v_cmp_ne_u32_e64 s[46:47], 0, v5
	v_cmp_ne_u32_e64 s[48:49], 0, v4
	v_cmp_ne_u32_e64 s[50:51], 0, v3
	v_cmp_ne_u32_e64 s[52:53], 0, v2
	v_addc_co_u32_e64 v44, s[54:55], v44, v44, s[46:47]
	v_addc_co_u32_e64 v44, s[54:55], v44, v44, s[48:49]
	v_addc_co_u32_e64 v44, s[54:55], v44, v44, s[50:51]
	v_addc_co_u32_e64 v44, s[54:55], v44, v44, s[52:53]
	s_lshl_b32 s80, s79, 7
	v_lshl_add_u32 v46, v126, 1, s80
	global_store_short v46, v44, s[36:37] sc1
